# v81 + routing: router-bias loads hoisted out of the token loop, per-token load waits removed
# speedup vs baseline: 1.0077x; 1.0008x over previous
.LBB0_578:
	s_or_b64 exec, exec, s[0:1]
	s_add_u32 s40, s70, 0x5440
	s_addc_u32 s41, s71, 0
	s_add_u32 s0, s70, 0x1260d500
	s_addc_u32 s1, s71, 0
	v_writelane_b32 v253, s0, 55
	s_waitcnt lgkmcnt(0)
	s_barrier
	v_writelane_b32 v253, s1, 56
	s_add_u32 s0, s70, 0x1268d500
	s_addc_u32 s1, s71, 0
	v_writelane_b32 v253, s0, 57
	v_mov_b32_e32 v1, 0
	s_nop 0
	v_writelane_b32 v253, s1, 58
	s_add_u32 s0, s70, 0x1270d500
	s_addc_u32 s1, s71, 0
	v_writelane_b32 v253, s0, 59
	v_mov_b32_e32 v3, 0
	s_movk_i32 s33, 0x4000
	v_writelane_b32 v253, s1, 60
	s_add_u32 s0, s70, 0x1278d500
	s_addc_u32 s1, s71, 0
	v_writelane_b32 v253, s0, 61
	s_nop 1
	v_writelane_b32 v253, s1, 62
	s_getreg_b32 s0, hwreg(HW_REG_HW_ID, 0, 6)
	s_lshl_b32 s0, s0, 2
	s_add_i32 s0, s0, 0x27000
	v_mov_b32_e32 v0, s0
	ds_read_b32 v0, v0
	s_waitcnt lgkmcnt(0)
	v_readfirstlane_b32 s0, v0
	v_mbcnt_lo_u32_b32 v0, -1, v1
	v_mbcnt_hi_u32_b32 v0, -1, v0
	v_lshl_or_b32 v0, s0, 6, v0
	s_getreg_b32 s0, hwreg(HW_REG_HW_ID, 0, 6)
	s_lshl_b32 s0, s0, 2
	s_add_i32 s0, s0, 0x27000
	v_mov_b32_e32 v1, s0
	ds_read_b32 v2, v1
	v_mov_b32_e32 v1, 0
	s_waitcnt lgkmcnt(0)
	v_readfirstlane_b32 s0, v2
	v_mbcnt_lo_u32_b32 v2, -1, v3
	v_mbcnt_hi_u32_b32 v2, -1, v2
	v_lshl_or_b32 v2, s0, 6, v2
	v_readlane_b32 s0, v253, 30
	v_ashrrev_i32_e32 v8, 6, v2
	s_nop 0
	v_add_u32_e32 v2, s0, v8
	v_cmp_gt_i32_e32 vcc, s33, v2
	s_and_saveexec_b64 s[44:45], vcc
	s_cbranch_execz .LBB0_667
	v_ashrrev_i32_e32 v3, 31, v2
	v_readlane_b32 s2, v253, 53
	v_and_b32_e32 v22, 63, v0
	v_lshlrev_b64 v[4:5], 10, v[2:3]
	v_readlane_b32 s3, v253, 54
	v_lshlrev_b32_e32 v0, 2, v22
	v_readlane_b32 s12, v253, 4
	v_lshl_add_u64 v[4:5], s[2:3], 0, v[4:5]
	v_lshl_add_u64 v[4:5], v[4:5], 0, v[0:1]
	global_load_dword v24, v[4:5], off
	global_load_dword v29, v[4:5], off offset:256
	global_load_dword v30, v[4:5], off offset:512
	global_load_dword v9, v[4:5], off offset:768
	v_readlane_b32 s13, v253, 5
	v_xor_b32_e32 v3, 64, v0
	v_xor_b32_e32 v23, 0x80, v0
	v_lshl_add_u64 v[4:5], s[12:13], 0, v[0:1]
	global_load_dword v61, v[4:5], off
	global_load_dword v62, v[4:5], off offset:256
	global_load_dword v63, v[4:5], off offset:512
	global_load_dword v64, v[4:5], off offset:768
	v_lshl_add_u64 v[6:7], s[2:3], 0, v[0:1]
	s_lshl_b32 s2, s72, 6
	v_lshlrev_b32_e32 v0, 3, v8
	v_readlane_b32 s14, v253, 6
	v_readlane_b32 s15, v253, 7
	v_readlane_b32 s16, v253, 8
	v_readlane_b32 s17, v253, 9
	v_readlane_b32 s18, v253, 10
	v_readlane_b32 s19, v253, 11
	v_readlane_b32 s20, v253, 12
	v_readlane_b32 s21, v253, 13
	v_readlane_b32 s22, v253, 14
	v_readlane_b32 s23, v253, 15
	v_readlane_b32 s24, v253, 16
	v_readlane_b32 s25, v253, 17
	v_add3_u32 v8, s2, v0, v22
	v_readlane_b32 s2, v253, 2
	v_cmp_gt_u32_e64 s[0:1], 32, v22
	v_cmp_lt_u32_e64 s[4:5], 31, v22
	v_cmp_lt_u32_e64 s[6:7], 7, v22
	v_cmp_gt_u32_e64 s[8:9], 8, v22
	v_cmp_eq_u32_e64 s[10:11], 0, v22
	v_cmp_eq_u32_e64 s[12:13], 1, v22
	v_cmp_eq_u32_e64 s[14:15], 2, v22
	v_cmp_eq_u32_e64 s[16:17], 3, v22
	v_cmp_eq_u32_e64 s[18:19], 4, v22
	v_cmp_eq_u32_e64 s[20:21], 5, v22
	v_cmp_eq_u32_e64 s[22:23], 6, v22
	v_cmp_eq_u32_e64 s[24:25], 7, v22
	s_lshl_b32 s52, s2, 6
	s_mov_b64 s[46:47], 0
	s_mov_b32 s53, 0xbfb8aa3b
	s_mov_b32 s54, 0x42ce8ed0
	s_mov_b32 s55, 0xc2b17218
	v_mov_b32_e32 v25, 0x7f800000
	v_mov_b32_e32 v26, 0xff800000
	v_mov_b32_e32 v27, 1
	v_readlane_b32 s26, v253, 18
	v_readlane_b32 s27, v253, 19
	v_readlane_b32 s3, v253, 3
	s_waitcnt vmcnt(0)
	s_branch .LBB0_581
.Lopt19_rt0_skip:
	s_waitcnt vmcnt(0)
.LBB0_580:
	s_or_b64 exec, exec, s[2:3]
	s_and_b64 s[2:3], exec, s[26:27]
	s_or_b64 s[46:47], s[2:3], s[46:47]
	v_add_u32_e32 v8, s52, v8
	v_mov_b32_e32 v2, v28
	v_mov_b32_e32 v9, v31
	s_andn2_b64 exec, exec, s[46:47]
	s_cbranch_execz .LBB0_667
.LBB0_581:
	v_add_u32_e32 v28, s74, v2
	v_cmp_gt_i32_e32 vcc, s33, v28
	v_mov_b32_e32 v12, v24
	v_mov_b32_e32 v13, v29
	v_cndmask_b32_e32 v10, v2, v28, vcc
	v_ashrrev_i32_e32 v11, 31, v10
	v_lshlrev_b64 v[10:11], 10, v[10:11]
	v_lshl_add_u64 v[18:19], v[6:7], 0, v[10:11]
	v_mul_f32_e32 v10, 0xbfb8aa3b, v12
	v_rndne_f32_e32 v11, v10
	v_sub_f32_e32 v14, v10, v11
	v_fma_f32 v10, v12, s53, -v10
	v_fmac_f32_e32 v10, 0xb2a5705f, v12
	v_add_f32_e32 v10, v14, v10
	v_exp_f32_e32 v10, v10
	v_cvt_i32_f32_e32 v11, v11
	v_cmp_nlt_f32_e32 vcc, s54, v12
	global_load_dword v24, v[18:19], off
	s_movk_i32 s2, 0x3fff
	v_ldexp_f32 v10, v10, v11
	v_mul_f32_e32 v11, 0xbfb8aa3b, v13
	v_rndne_f32_e32 v14, v11
	v_sub_f32_e32 v15, v11, v14
	v_fma_f32 v11, v13, s53, -v11
	v_fmac_f32_e32 v11, 0xb2a5705f, v13
	v_add_f32_e32 v11, v15, v11
	v_exp_f32_e32 v11, v11
	v_cvt_i32_f32_e32 v14, v14
	v_cndmask_b32_e32 v10, 0, v10, vcc
	v_cmp_ngt_f32_e32 vcc, s55, v12
	v_mov_b32_e32 v12, v61
	global_load_dword v29, v[18:19], off offset:256
	v_cndmask_b32_e32 v10, v25, v10, vcc
	v_ldexp_f32 v11, v11, v14
	v_cmp_nlt_f32_e32 vcc, s54, v13
	v_cmp_lt_i32_e64 s[26:27], s2, v28
	v_mov_b32_e32 v0, v30
	v_cndmask_b32_e32 v11, 0, v11, vcc
	v_cmp_ngt_f32_e32 vcc, s55, v13
	v_mov_b32_e32 v13, v62
	global_load_dword v30, v[18:19], off offset:512
	v_cndmask_b32_e32 v11, v25, v11, vcc
	v_pk_add_f32 v[10:11], v[10:11], 1.0 op_sel_hi:[1,0]
	s_nop 0
	v_div_scale_f32 v14, s[2:3], v11, v11, 1.0
	v_rcp_f32_e32 v15, v14
	s_nop 0
	v_fma_f32 v16, -v14, v15, 1.0
	v_fmac_f32_e32 v15, v16, v15
	v_div_scale_f32 v16, vcc, 1.0, v11, 1.0
	v_mul_f32_e32 v17, v16, v15
	v_fma_f32 v20, -v14, v17, v16
	v_fmac_f32_e32 v17, v20, v15
	v_fma_f32 v14, -v14, v17, v16
	v_div_fmas_f32 v14, v14, v15, v17
	v_div_fixup_f32 v11, v14, v11, 1.0
	v_div_scale_f32 v14, s[2:3], v10, v10, 1.0
	v_rcp_f32_e32 v15, v14
	s_nop 0
	v_fma_f32 v16, -v14, v15, 1.0
	v_fmac_f32_e32 v15, v16, v15
	v_div_scale_f32 v16, vcc, 1.0, v10, 1.0
	v_mul_f32_e32 v17, v16, v15
	v_fma_f32 v20, -v14, v17, v16
	v_fmac_f32_e32 v17, v20, v15
	v_fma_f32 v14, -v14, v17, v16
	v_div_fmas_f32 v14, v14, v15, v17
	v_div_fixup_f32 v10, v14, v10, 1.0
	v_cmp_nlt_f32_e32 vcc, s54, v0
	v_pk_add_f32 v[14:15], v[12:13], v[10:11]
	v_mul_f32_e32 v12, 0xbfb8aa3b, v0
	v_rndne_f32_e32 v13, v12
	v_sub_f32_e32 v16, v12, v13
	v_fma_f32 v12, v0, s53, -v12
	v_fmac_f32_e32 v12, 0xb2a5705f, v0
	v_add_f32_e32 v12, v16, v12
	v_exp_f32_e32 v12, v12
	v_cvt_i32_f32_e32 v13, v13
	v_mov_b32_e32 v16, v63
	global_load_dword v31, v[18:19], off offset:768
	v_ldexp_f32 v12, v12, v13
	v_cndmask_b32_e32 v12, 0, v12, vcc
	v_cmp_ngt_f32_e32 vcc, s55, v0
	v_mul_f32_e32 v0, 0xbfb8aa3b, v9
	v_rndne_f32_e32 v13, v0
	v_sub_f32_e32 v17, v0, v13
	v_fma_f32 v0, v9, s53, -v0
	v_fmac_f32_e32 v0, 0xb2a5705f, v9
	v_add_f32_e32 v0, v17, v0
	v_mov_b32_e32 v17, v64
	v_exp_f32_e32 v0, v0
	v_cvt_i32_f32_e32 v13, v13
	v_cndmask_b32_e32 v12, v25, v12, vcc
	v_cmp_nlt_f32_e32 vcc, s54, v9
	v_ldexp_f32 v0, v0, v13
	s_nop 0
	v_cndmask_b32_e32 v0, 0, v0, vcc
	v_cmp_ngt_f32_e32 vcc, s55, v9
	s_nop 1
	v_cndmask_b32_e32 v13, v25, v0, vcc
	v_pk_add_f32 v[12:13], v[12:13], 1.0 op_sel_hi:[1,0]
	s_nop 0
	v_div_scale_f32 v0, s[2:3], v13, v13, 1.0
	v_rcp_f32_e32 v9, v0
	s_nop 0
	v_fma_f32 v18, -v0, v9, 1.0
	v_fmac_f32_e32 v9, v18, v9
	v_div_scale_f32 v18, vcc, 1.0, v13, 1.0
	v_mul_f32_e32 v19, v18, v9
	v_fma_f32 v20, -v0, v19, v18
	v_fmac_f32_e32 v19, v20, v9
	v_fma_f32 v0, -v0, v19, v18
	v_div_fmas_f32 v0, v0, v9, v19
	v_div_fixup_f32 v13, v0, v13, 1.0
	v_div_scale_f32 v0, s[2:3], v12, v12, 1.0
	v_rcp_f32_e32 v9, v0
	s_nop 0
	v_fma_f32 v18, -v0, v9, 1.0
	v_fmac_f32_e32 v9, v18, v9
	v_div_scale_f32 v18, vcc, 1.0, v12, 1.0
	v_mul_f32_e32 v19, v18, v9
	v_fma_f32 v20, -v0, v19, v18
	v_fmac_f32_e32 v19, v20, v9
	v_fma_f32 v0, -v0, v19, v18
	v_div_fmas_f32 v0, v0, v9, v19
	v_div_fixup_f32 v12, v0, v12, 1.0
	v_mov_b32_dpp v9, v26 quad_perm:[1,0,3,2] row_mask:0xf bank_mask:0xf bound_ctrl:1
	v_mov_b32_dpp v0, v14 quad_perm:[1,0,3,2] row_mask:0xf bank_mask:0xf bound_ctrl:1
	v_max_f32_e32 v0, v0, v0
	v_max_f32_e32 v9, v9, v9
	v_min_f32_e32 v18, v14, v0
	v_max_f32_e32 v0, v14, v0
	v_max_f32_e32 v21, 0xff800000, v9
	v_max_f32_e32 v9, v18, v21
	v_mov_b32_dpp v18, v0 quad_perm:[2,3,0,1] row_mask:0xf bank_mask:0xf bound_ctrl:1
	v_max_f32_e32 v18, v18, v18
	v_min_f32_e32 v20, v0, v18
	v_max_f32_e32 v0, v0, v18
	v_mov_b32_dpp v19, v9 quad_perm:[2,3,0,1] row_mask:0xf bank_mask:0xf bound_ctrl:1
	v_max3_f32 v9, v20, v9, v19
	v_mov_b32_dpp v18, v0 row_half_mirror row_mask:0xf bank_mask:0xf bound_ctrl:1
	v_max_f32_e32 v18, v18, v18
	v_min_f32_e32 v20, v0, v18
	v_max_f32_e32 v0, v0, v18
	v_mov_b32_dpp v19, v9 row_half_mirror row_mask:0xf bank_mask:0xf bound_ctrl:1
	v_max3_f32 v9, v20, v9, v19
	v_mov_b32_dpp v18, v0 row_mirror row_mask:0xf bank_mask:0xf bound_ctrl:1
	v_max_f32_e32 v18, v18, v18
	v_min_f32_e32 v20, v0, v18
	v_max_f32_e32 v0, v0, v18
	ds_bpermute_b32 v18, v3, v0
	v_mov_b32_dpp v19, v9 row_mirror row_mask:0xf bank_mask:0xf bound_ctrl:1
	v_max3_f32 v9, v20, v9, v19
	ds_bpermute_b32 v19, v3, v9
	s_waitcnt lgkmcnt(1)
	v_max_f32_e32 v18, v18, v18
	v_min_f32_e32 v32, v0, v18
	v_max_f32_e32 v20, v0, v18
	v_mov_b32_dpp v0, v15 quad_perm:[1,0,3,2] row_mask:0xf bank_mask:0xf bound_ctrl:1
	v_max_f32_e32 v0, v0, v0
	s_waitcnt lgkmcnt(0)
	v_max3_f32 v32, v32, v9, v19
	v_min_f32_e32 v9, v15, v0
	v_max_f32_e32 v0, v15, v0
	v_max_f32_e32 v9, v9, v21
	v_pk_add_f32 v[16:17], v[12:13], v[16:17]
	v_mov_b32_dpp v18, v0 quad_perm:[2,3,0,1] row_mask:0xf bank_mask:0xf bound_ctrl:1
	v_max_f32_e32 v18, v18, v18
	v_min_f32_e32 v33, v0, v18
	v_max_f32_e32 v0, v0, v18
	v_mov_b32_dpp v19, v9 quad_perm:[2,3,0,1] row_mask:0xf bank_mask:0xf bound_ctrl:1
	v_max3_f32 v9, v33, v9, v19
	v_mov_b32_dpp v18, v0 row_half_mirror row_mask:0xf bank_mask:0xf bound_ctrl:1
	v_max_f32_e32 v18, v18, v18
	v_min_f32_e32 v33, v0, v18
	v_max_f32_e32 v0, v0, v18
	v_mov_b32_dpp v19, v9 row_half_mirror row_mask:0xf bank_mask:0xf bound_ctrl:1
	v_max3_f32 v9, v33, v9, v19
	v_mov_b32_dpp v18, v0 row_mirror row_mask:0xf bank_mask:0xf bound_ctrl:1
	v_max_f32_e32 v18, v18, v18
	v_min_f32_e32 v33, v0, v18
	v_max_f32_e32 v0, v0, v18
	ds_bpermute_b32 v18, v3, v0
	v_mov_b32_dpp v19, v9 row_mirror row_mask:0xf bank_mask:0xf bound_ctrl:1
	v_max3_f32 v9, v33, v9, v19
	ds_bpermute_b32 v19, v3, v9
	s_waitcnt lgkmcnt(1)
	v_max_f32_e32 v18, v18, v18
	v_min_f32_e32 v33, v0, v18
	v_max_f32_e32 v18, v0, v18
	v_mov_b32_dpp v0, v16 quad_perm:[1,0,3,2] row_mask:0xf bank_mask:0xf bound_ctrl:1
	v_max_f32_e32 v0, v0, v0
	s_waitcnt lgkmcnt(0)
	v_max3_f32 v34, v33, v9, v19
	v_min_f32_e32 v9, v16, v0
	v_max_f32_e32 v0, v16, v0
	v_max_f32_e32 v9, v9, v21
	s_nop 0
	v_mov_b32_dpp v19, v0 quad_perm:[2,3,0,1] row_mask:0xf bank_mask:0xf bound_ctrl:1
	v_max_f32_e32 v19, v19, v19
	v_min_f32_e32 v35, v0, v19
	v_max_f32_e32 v0, v0, v19
	v_mov_b32_dpp v33, v9 quad_perm:[2,3,0,1] row_mask:0xf bank_mask:0xf bound_ctrl:1
	v_max3_f32 v9, v35, v9, v33
	v_mov_b32_dpp v19, v0 row_half_mirror row_mask:0xf bank_mask:0xf bound_ctrl:1
	v_max_f32_e32 v19, v19, v19
	v_min_f32_e32 v35, v0, v19
	v_max_f32_e32 v0, v0, v19
	v_mov_b32_dpp v33, v9 row_half_mirror row_mask:0xf bank_mask:0xf bound_ctrl:1
	v_max3_f32 v9, v35, v9, v33
	v_mov_b32_dpp v19, v0 row_mirror row_mask:0xf bank_mask:0xf bound_ctrl:1
	v_max_f32_e32 v19, v19, v19
	v_min_f32_e32 v35, v0, v19
	v_max_f32_e32 v0, v0, v19
	v_mov_b32_dpp v33, v9 row_mirror row_mask:0xf bank_mask:0xf bound_ctrl:1
	ds_bpermute_b32 v19, v3, v0
	v_max3_f32 v9, v35, v9, v33
	ds_bpermute_b32 v33, v3, v9
	s_waitcnt lgkmcnt(1)
	v_max_f32_e32 v19, v19, v19
	v_min_f32_e32 v35, v0, v19
	s_waitcnt lgkmcnt(0)
	v_max3_f32 v35, v35, v9, v33
	v_mov_b32_dpp v33, v17 quad_perm:[1,0,3,2] row_mask:0xf bank_mask:0xf bound_ctrl:1
	v_max_f32_e32 v19, v0, v19
	v_max_f32_e32 v33, v33, v33
	v_pk_add_f32 v[18:19], v[18:19], v[34:35]
	v_min_f32_e32 v34, v17, v33
	v_max_f32_e32 v33, v17, v33
	v_max_f32_e32 v21, v34, v21
	ds_bpermute_b32 v9, v23, v18
	v_mov_b32_dpp v34, v33 quad_perm:[2,3,0,1] row_mask:0xf bank_mask:0xf bound_ctrl:1
	v_max_f32_e32 v34, v34, v34
	v_min_f32_e32 v36, v33, v34
	v_max_f32_e32 v33, v33, v34
	v_mov_b32_dpp v35, v21 quad_perm:[2,3,0,1] row_mask:0xf bank_mask:0xf bound_ctrl:1
	v_max3_f32 v21, v36, v21, v35
	v_mov_b32_dpp v34, v33 row_half_mirror row_mask:0xf bank_mask:0xf bound_ctrl:1
	v_max_f32_e32 v34, v34, v34
	v_min_f32_e32 v36, v33, v34
	v_max_f32_e32 v33, v33, v34
	v_mov_b32_dpp v35, v21 row_half_mirror row_mask:0xf bank_mask:0xf bound_ctrl:1
	v_max3_f32 v21, v36, v21, v35
	v_mov_b32_dpp v34, v33 row_mirror row_mask:0xf bank_mask:0xf bound_ctrl:1
	v_max_f32_e32 v34, v34, v34
	v_mov_b32_dpp v35, v21 row_mirror row_mask:0xf bank_mask:0xf bound_ctrl:1
	v_min_f32_e32 v36, v33, v34
	v_max_f32_e32 v33, v33, v34
	v_max3_f32 v34, v36, v21, v35
	ds_bpermute_b32 v21, v3, v33
	ds_bpermute_b32 v35, v3, v34
	ds_bpermute_b32 v0, v23, v19
	s_waitcnt lgkmcnt(2)
	v_max_f32_e32 v21, v21, v21
	v_min_f32_e32 v36, v33, v21
	v_max_f32_e32 v21, v33, v21
	s_waitcnt lgkmcnt(1)
	v_max3_f32 v33, v36, v34, v35
	v_pk_add_f32 v[20:21], v[20:21], v[32:33]
	ds_bpermute_b32 v34, v23, v20
	ds_bpermute_b32 v32, v23, v21
	s_and_saveexec_b64 s[28:29], s[4:5]
	s_xor_b64 s[28:29], exec, s[28:29]
	s_cbranch_execz .LBB0_583
	s_waitcnt lgkmcnt(1)
	v_cmp_le_f32_e32 vcc, v21, v34
	v_cmp_le_f32_e64 s[2:3], v20, v34
	s_nop 0
	v_cndmask_b32_e64 v33, 0, 1, vcc
	v_cmp_ge_f32_e32 vcc, v20, v21
	s_nop 1
	v_cndmask_b32_e64 v35, 0, 1, vcc
	v_cmp_le_f32_e32 vcc, v21, v9
	s_nop 1
	v_addc_co_u32_e32 v33, vcc, v33, v35, vcc
	v_cmp_ge_f32_e32 vcc, v18, v21
	s_nop 1
	v_cndmask_b32_e64 v35, 0, 1, vcc
	v_cmp_le_f32_e32 vcc, v21, v0
	s_nop 1
	v_addc_co_u32_e32 v33, vcc, v33, v35, vcc
	v_cmp_ge_f32_e32 vcc, v19, v21
	s_nop 1
	v_cndmask_b32_e64 v35, 0, 1, vcc
	s_waitcnt lgkmcnt(0)
	v_cmp_le_f32_e32 vcc, v21, v32
	s_nop 1
	v_addc_co_u32_e32 v33, vcc, v33, v35, vcc
	v_cmp_le_f32_e32 vcc, v19, v34
	s_nop 1
	v_cndmask_b32_e64 v35, 0, 1, vcc
	v_cmp_ge_f32_e32 vcc, v20, v19
	s_nop 1
	v_cndmask_b32_e64 v36, 0, 1, vcc
	v_cmp_le_f32_e32 vcc, v19, v9
	s_nop 1
	v_addc_co_u32_e32 v35, vcc, v35, v36, vcc
	v_cmp_ge_f32_e32 vcc, v18, v19
	s_nop 1
	v_cndmask_b32_e64 v36, 0, 1, vcc
	v_cmp_le_f32_e32 vcc, v19, v0
	s_nop 1
	v_addc_co_u32_e32 v35, vcc, v35, v36, vcc
	v_cmp_lt_f32_e32 vcc, v19, v32
	s_nop 1
	v_cndmask_b32_e64 v36, 0, 1, vcc
	v_cmp_gt_f32_e32 vcc, v21, v19
	s_nop 1
	v_addc_co_u32_e32 v35, vcc, v35, v36, vcc
	v_cmp_le_f32_e32 vcc, v18, v34
	s_nop 1
	v_cndmask_b32_e64 v34, 0, 1, vcc
	v_cmp_ge_f32_e32 vcc, v20, v18
	s_nop 1
	v_cndmask_b32_e64 v36, 0, 1, vcc
	v_cmp_le_f32_e32 vcc, v18, v9
	s_nop 1
	v_addc_co_u32_e32 v34, vcc, v34, v36, vcc
	v_cmp_lt_f32_e32 vcc, v18, v0
	s_nop 1
	v_cndmask_b32_e64 v36, 0, 1, vcc
	v_cmp_gt_f32_e32 vcc, v19, v18
	s_nop 1
	v_addc_co_u32_e32 v34, vcc, v34, v36, vcc
	v_cmp_lt_f32_e32 vcc, v18, v32
	s_nop 1
	v_cndmask_b32_e64 v36, 0, 1, vcc
	v_cmp_gt_f32_e32 vcc, v21, v18
	s_nop 1
	v_addc_co_u32_e32 v36, vcc, v34, v36, vcc

.LBB0_2160:
	s_or_b64 exec, exec, s[0:1]
	s_waitcnt lgkmcnt(0)
	s_barrier
	s_add_u32 s30, s70, 0x9440
	s_getreg_b32 s0, hwreg(HW_REG_HW_ID, 0, 6)
	s_addc_u32 s31, s71, 0
	s_lshl_b32 s0, s0, 2
	s_add_i32 s0, s0, 0x27000
	v_mov_b32_e32 v0, s0
	ds_read_b32 v0, v0
	v_mov_b32_e32 v1, 0
	v_mov_b32_e32 v3, 0
	s_movk_i32 s33, 0x4000
	s_waitcnt lgkmcnt(0)
	v_readfirstlane_b32 s0, v0
	v_mbcnt_lo_u32_b32 v0, -1, v1
	v_mbcnt_hi_u32_b32 v0, -1, v0
	v_lshl_or_b32 v0, s0, 6, v0
	s_getreg_b32 s0, hwreg(HW_REG_HW_ID, 0, 6)
	s_lshl_b32 s0, s0, 2
	s_add_i32 s0, s0, 0x27000
	v_mov_b32_e32 v1, s0
	ds_read_b32 v2, v1
	v_mov_b32_e32 v1, 0
	s_waitcnt lgkmcnt(0)
	v_readfirstlane_b32 s0, v2
	v_mbcnt_lo_u32_b32 v2, -1, v3
	v_mbcnt_hi_u32_b32 v2, -1, v2
	v_lshl_or_b32 v2, s0, 6, v2
	v_readlane_b32 s0, v253, 30
	v_ashrrev_i32_e32 v8, 6, v2
	s_nop 0
	v_add_u32_e32 v2, s0, v8
	v_cmp_gt_i32_e32 vcc, s33, v2
	s_and_saveexec_b64 s[34:35], vcc
	s_cbranch_execz .LBB0_2249
	v_ashrrev_i32_e32 v3, 31, v2
	v_readlane_b32 s24, v253, 53
	v_and_b32_e32 v22, 63, v0
	v_lshlrev_b64 v[4:5], 10, v[2:3]
	v_readlane_b32 s25, v253, 54
	v_lshlrev_b32_e32 v0, 2, v22
	v_readlane_b32 s8, v253, 4
	v_lshl_add_u64 v[4:5], s[24:25], 0, v[4:5]
	v_lshl_add_u64 v[4:5], v[4:5], 0, v[0:1]
	global_load_dword v28, v[4:5], off
	global_load_dword v29, v[4:5], off offset:256
	global_load_dword v30, v[4:5], off offset:512
	global_load_dword v31, v[4:5], off offset:768
	v_readlane_b32 s9, v253, 5
	v_xor_b32_e32 v3, 64, v0
	v_xor_b32_e32 v23, 0x80, v0
	v_lshl_add_u64 v[4:5], s[8:9], 0, v[0:1]
	global_load_dword v61, v[4:5], off offset:1024
	global_load_dword v62, v[4:5], off offset:1280
	global_load_dword v63, v[4:5], off offset:1536
	global_load_dword v64, v[4:5], off offset:1792
	v_lshl_add_u64 v[6:7], s[24:25], 0, v[0:1]
	s_lshl_b32 s24, s72, 6
	v_lshlrev_b32_e32 v0, 3, v8
	v_readlane_b32 s10, v253, 6
	v_readlane_b32 s11, v253, 7
	v_readlane_b32 s12, v253, 8
	v_readlane_b32 s13, v253, 9
	v_readlane_b32 s14, v253, 10
	v_readlane_b32 s15, v253, 11
	v_readlane_b32 s16, v253, 12
	v_readlane_b32 s17, v253, 13
	v_readlane_b32 s18, v253, 14
	v_readlane_b32 s19, v253, 15
	v_readlane_b32 s20, v253, 16
	v_readlane_b32 s21, v253, 17
	v_readlane_b32 s22, v253, 18
	v_readlane_b32 s23, v253, 19
	v_add3_u32 v8, s24, v0, v22
	v_readlane_b32 s24, v253, 2
	v_cmp_gt_u32_e64 s[0:1], 32, v22
	v_cmp_lt_u32_e64 s[2:3], 31, v22
	v_cmp_lt_u32_e64 s[4:5], 7, v22
	v_cmp_gt_u32_e64 s[6:7], 8, v22
	v_cmp_eq_u32_e64 s[8:9], 0, v22
	v_cmp_eq_u32_e64 s[10:11], 1, v22
	v_cmp_eq_u32_e64 s[12:13], 2, v22
	v_cmp_eq_u32_e64 s[14:15], 3, v22
	v_cmp_eq_u32_e64 s[16:17], 4, v22
	v_cmp_eq_u32_e64 s[18:19], 5, v22
	v_cmp_eq_u32_e64 s[20:21], 6, v22
	v_cmp_eq_u32_e64 s[22:23], 7, v22
	s_lshl_b32 s42, s24, 6
	s_mov_b64 s[36:37], 0
	s_movk_i32 s43, 0x3fff
	s_mov_b32 s44, 0xbfb8aa3b
	s_mov_b32 s45, 0x42ce8ed0
	s_mov_b32 s46, 0xc2b17218
	v_mov_b32_e32 v24, 0x7f800000
	v_mov_b32_e32 v25, 0xff800000
	s_mov_b32 s47, 0xff800000
	v_mov_b32_e32 v26, 1
	v_readlane_b32 s25, v253, 3
	s_waitcnt vmcnt(0)
	s_branch .LBB0_2163
.Lopt19_rt1_skip:
	s_waitcnt vmcnt(0)
.LBB0_2162:
	s_or_b64 exec, exec, s[26:27]
	s_and_b64 s[24:25], exec, s[24:25]
	s_or_b64 s[36:37], s[24:25], s[36:37]
	v_add_u32_e32 v8, s42, v8
	v_mov_b32_e32 v2, v27
	s_andn2_b64 exec, exec, s[36:37]
	s_cbranch_execz .LBB0_2249
.LBB0_2163:
	v_mov_b32_e32 v12, v61
	v_mov_b32_e32 v13, v62
	v_mul_f32_e32 v9, 0xbfb8aa3b, v28
	v_mul_f32_e32 v14, 0xbfb8aa3b, v29
	v_rndne_f32_e32 v18, v9
	v_fma_f32 v19, v28, s44, -v9
	v_rndne_f32_e32 v21, v14
	v_fma_f32 v32, v29, s44, -v14
	v_sub_f32_e32 v9, v9, v18
	v_fmac_f32_e32 v19, 0xb2a5705f, v28
	v_sub_f32_e32 v14, v14, v21
	v_fmac_f32_e32 v32, 0xb2a5705f, v29
	v_add_f32_e32 v9, v9, v19
	v_add_u32_e32 v27, s74, v2
	v_cvt_i32_f32_e32 v36, v18
	v_add_f32_e32 v14, v14, v32
	v_exp_f32_e32 v9, v9
	v_cmp_gt_i32_e32 vcc, s33, v27
	v_cvt_i32_f32_e32 v21, v21
	v_exp_f32_e32 v14, v14
	v_cndmask_b32_e32 v10, v2, v27, vcc
	v_mul_f32_e32 v15, 0xbfb8aa3b, v30
	v_ashrrev_i32_e32 v11, 31, v10
	v_rndne_f32_e32 v33, v15
	v_fma_f32 v34, v30, s44, -v15
	v_lshlrev_b64 v[10:11], 10, v[10:11]
	v_ldexp_f32 v9, v9, v36
	v_cmp_nlt_f32_e32 vcc, s45, v28
	v_sub_f32_e32 v15, v15, v33
	v_fmac_f32_e32 v34, 0xb2a5705f, v30
	v_lshl_add_u64 v[18:19], v[6:7], 0, v[10:11]
	v_ldexp_f32 v10, v14, v21
	v_cndmask_b32_e32 v9, 0, v9, vcc
	v_cmp_nlt_f32_e32 vcc, s45, v29
	v_add_f32_e32 v15, v15, v34
	v_cvt_i32_f32_e32 v33, v33
	v_cndmask_b32_e32 v11, 0, v10, vcc
	v_cmp_ngt_f32_e32 vcc, s46, v28
	v_exp_f32_e32 v15, v15
	v_mov_b32_e32 v16, v63
	v_mov_b32_e32 v17, v64
	v_cndmask_b32_e32 v10, v24, v9, vcc
	v_cmp_ngt_f32_e32 vcc, s46, v29
	v_ldexp_f32 v21, v15, v33
	v_mul_f32_e32 v0, 0xbfb8aa3b, v31
	v_cndmask_b32_e32 v11, v24, v11, vcc
	v_pk_add_f32 v[10:11], v[10:11], 1.0 op_sel_hi:[1,0]
	v_rndne_f32_e32 v20, v0
	v_div_scale_f32 v9, s[24:25], v11, v11, 1.0
	v_div_scale_f32 v15, s[24:25], v10, v10, 1.0
	v_rcp_f32_e32 v28, v9
	v_rcp_f32_e32 v29, v15
	v_div_scale_f32 v14, vcc, 1.0, v11, 1.0
	v_fma_f32 v33, -v9, v28, 1.0
	v_fma_f32 v34, -v15, v29, 1.0
	v_fmac_f32_e32 v28, v33, v28
	v_div_scale_f32 v32, s[24:25], 1.0, v10, 1.0
	v_fmac_f32_e32 v29, v34, v29
	v_mul_f32_e32 v33, v14, v28
	v_mul_f32_e32 v34, v32, v29
	v_fma_f32 v36, -v9, v33, v14
	v_fma_f32 v37, -v15, v34, v32
	v_fmac_f32_e32 v33, v36, v28
	v_sub_f32_e32 v35, v0, v20
	v_fmac_f32_e32 v34, v37, v29
	v_fma_f32 v9, -v9, v33, v14
	v_fma_f32 v0, v31, s44, -v0
	v_fma_f32 v14, -v15, v34, v32
	v_div_fmas_f32 v9, v9, v28, v33
	s_mov_b64 vcc, s[24:25]
	v_fmac_f32_e32 v0, 0xb2a5705f, v31
	v_div_fixup_f32 v11, v9, v11, 1.0
	v_div_fmas_f32 v9, v14, v29, v34
	v_add_f32_e32 v0, v35, v0
	v_div_fixup_f32 v10, v9, v10, 1.0
	v_exp_f32_e32 v0, v0
	v_cvt_i32_f32_e32 v9, v20
	v_cmp_nlt_f32_e32 vcc, s45, v30
	v_pk_add_f32 v[14:15], v[12:13], v[10:11]
	v_ldexp_f32 v0, v0, v9
	v_cndmask_b32_e32 v12, 0, v21, vcc
	v_cmp_ngt_f32_e32 vcc, s46, v30
	s_nop 1
	v_cndmask_b32_e32 v12, v24, v12, vcc
	v_cmp_nlt_f32_e32 vcc, s45, v31
	s_nop 1
	v_cndmask_b32_e32 v0, 0, v0, vcc
	v_cmp_ngt_f32_e32 vcc, s46, v31
	global_load_dword v28, v[18:19], off
	global_load_dword v29, v[18:19], off offset:256
	global_load_dword v30, v[18:19], off offset:512
	global_load_dword v31, v[18:19], off offset:768
	v_cndmask_b32_e32 v13, v24, v0, vcc
	v_pk_add_f32 v[12:13], v[12:13], 1.0 op_sel_hi:[1,0]
	s_nop 0
	v_div_scale_f32 v0, s[24:25], v13, v13, 1.0
	v_rcp_f32_e32 v9, v0
	s_nop 0
	v_fma_f32 v18, -v0, v9, 1.0
	v_fmac_f32_e32 v9, v18, v9
	v_div_scale_f32 v18, vcc, 1.0, v13, 1.0
	v_mul_f32_e32 v19, v18, v9
	v_fma_f32 v20, -v0, v19, v18
	v_fmac_f32_e32 v19, v20, v9
	v_fma_f32 v0, -v0, v19, v18
	v_div_scale_f32 v18, s[24:25], v12, v12, 1.0
	v_rcp_f32_e32 v20, v18
	v_div_fmas_f32 v0, v0, v9, v19
	v_div_fixup_f32 v13, v0, v13, 1.0
	v_cmp_lt_i32_e64 s[24:25], s43, v27
	v_fma_f32 v0, -v18, v20, 1.0
	v_fmac_f32_e32 v20, v0, v20
	v_div_scale_f32 v0, vcc, 1.0, v12, 1.0
	v_mul_f32_e32 v9, v0, v20
	v_fma_f32 v19, -v18, v9, v0
	v_fmac_f32_e32 v9, v19, v20
	v_fma_f32 v0, -v18, v9, v0
	v_div_fmas_f32 v0, v0, v20, v9
	v_div_fixup_f32 v12, v0, v12, 1.0
	v_mov_b32_dpp v9, v25 quad_perm:[1,0,3,2] row_mask:0xf bank_mask:0xf bound_ctrl:1
	v_mov_b32_dpp v0, v14 quad_perm:[1,0,3,2] row_mask:0xf bank_mask:0xf bound_ctrl:1
	v_max_f32_e32 v0, v0, v0
	v_min_f32_e32 v18, v14, v0
	v_max_f32_e32 v0, v14, v0
	v_max_f32_e32 v9, v9, v9
	v_max_f32_e32 v9, 0xff800000, v9
	v_mov_b32_dpp v19, v0 quad_perm:[2,3,0,1] row_mask:0xf bank_mask:0xf bound_ctrl:1
	v_max_f32_e32 v19, v19, v19
	v_min_f32_e32 v21, v0, v19
	v_max_f32_e32 v0, v0, v19
	v_max_f32_e32 v18, v18, v9
	v_pk_add_f32 v[16:17], v[12:13], v[16:17]
	v_mov_b32_dpp v19, v0 row_half_mirror row_mask:0xf bank_mask:0xf bound_ctrl:1
	v_mov_b32_dpp v20, v18 quad_perm:[2,3,0,1] row_mask:0xf bank_mask:0xf bound_ctrl:1
	v_max_f32_e32 v19, v19, v19
	v_max3_f32 v18, v21, v18, v20
	v_min_f32_e32 v21, v0, v19
	v_max_f32_e32 v0, v0, v19
	v_mov_b32_dpp v20, v18 row_half_mirror row_mask:0xf bank_mask:0xf bound_ctrl:1
	v_max3_f32 v18, v21, v18, v20
	v_mov_b32_dpp v19, v0 row_mirror row_mask:0xf bank_mask:0xf bound_ctrl:1
	v_max_f32_e32 v19, v19, v19
	v_max_f32_e32 v21, v0, v19
	v_mov_b32_dpp v20, v18 row_mirror row_mask:0xf bank_mask:0xf bound_ctrl:1
	ds_bpermute_b32 v32, v3, v21
	v_min_f32_e32 v0, v0, v19
	v_max3_f32 v0, v0, v18, v20
	ds_bpermute_b32 v18, v3, v0
	s_waitcnt lgkmcnt(1)
	v_max_f32_e32 v19, v32, v32
	v_min_f32_e32 v32, v21, v19
	v_max_f32_e32 v20, v21, v19
	s_waitcnt lgkmcnt(0)
	v_max3_f32 v32, v32, v0, v18
	v_mov_b32_dpp v0, v15 quad_perm:[1,0,3,2] row_mask:0xf bank_mask:0xf bound_ctrl:1
	v_max_f32_e32 v0, v0, v0
	v_min_f32_e32 v18, v15, v0
	v_max_f32_e32 v0, v15, v0
	v_max_f32_e32 v18, v18, v9
	s_nop 0
	v_mov_b32_dpp v19, v0 quad_perm:[2,3,0,1] row_mask:0xf bank_mask:0xf bound_ctrl:1
	v_max_f32_e32 v19, v19, v19
	v_min_f32_e32 v33, v0, v19
	v_max_f32_e32 v0, v0, v19
	v_mov_b32_dpp v21, v18 quad_perm:[2,3,0,1] row_mask:0xf bank_mask:0xf bound_ctrl:1
	v_max3_f32 v18, v33, v18, v21
	v_mov_b32_dpp v19, v0 row_half_mirror row_mask:0xf bank_mask:0xf bound_ctrl:1
	v_max_f32_e32 v19, v19, v19
	v_min_f32_e32 v33, v0, v19
	v_max_f32_e32 v0, v0, v19
	v_mov_b32_dpp v21, v18 row_half_mirror row_mask:0xf bank_mask:0xf bound_ctrl:1
	v_max3_f32 v18, v33, v18, v21
	v_mov_b32_dpp v19, v0 row_mirror row_mask:0xf bank_mask:0xf bound_ctrl:1
	v_max_f32_e32 v19, v19, v19
	v_max_f32_e32 v21, v0, v19
	ds_bpermute_b32 v33, v3, v21
	v_mov_b32_dpp v34, v18 row_mirror row_mask:0xf bank_mask:0xf bound_ctrl:1
	v_min_f32_e32 v0, v0, v19
	v_max3_f32 v0, v0, v18, v34
	ds_bpermute_b32 v19, v3, v0
	s_waitcnt lgkmcnt(1)
	v_max_f32_e32 v18, v33, v33
	v_min_f32_e32 v33, v21, v18
	v_max_f32_e32 v18, v21, v18
	v_mov_b32_dpp v21, v16 quad_perm:[1,0,3,2] row_mask:0xf bank_mask:0xf bound_ctrl:1
	v_max_f32_e32 v21, v21, v21
	v_min_f32_e32 v34, v16, v21
	v_max_f32_e32 v21, v16, v21
	v_max_f32_e32 v34, v34, v9
	s_nop 0
	v_mov_b32_dpp v35, v21 quad_perm:[2,3,0,1] row_mask:0xf bank_mask:0xf bound_ctrl:1
	v_max_f32_e32 v35, v35, v35
	v_min_f32_e32 v37, v21, v35
	v_max_f32_e32 v21, v21, v35
	v_mov_b32_dpp v36, v34 quad_perm:[2,3,0,1] row_mask:0xf bank_mask:0xf bound_ctrl:1
	v_max3_f32 v34, v37, v34, v36
	v_mov_b32_dpp v35, v21 row_half_mirror row_mask:0xf bank_mask:0xf bound_ctrl:1
	v_max_f32_e32 v35, v35, v35
	v_min_f32_e32 v37, v21, v35
	v_max_f32_e32 v21, v21, v35
	v_mov_b32_dpp v36, v34 row_half_mirror row_mask:0xf bank_mask:0xf bound_ctrl:1
	v_max3_f32 v34, v37, v34, v36
	v_mov_b32_dpp v35, v21 row_mirror row_mask:0xf bank_mask:0xf bound_ctrl:1
	v_max_f32_e32 v35, v35, v35
	v_max_f32_e32 v37, v21, v35
	v_mov_b32_dpp v36, v34 row_mirror row_mask:0xf bank_mask:0xf bound_ctrl:1
	ds_bpermute_b32 v38, v3, v37
	v_min_f32_e32 v21, v21, v35
	v_max3_f32 v21, v21, v34, v36
	ds_bpermute_b32 v35, v3, v21
	s_waitcnt lgkmcnt(2)
	v_max3_f32 v34, v33, v0, v19
	s_waitcnt lgkmcnt(1)
	v_max_f32_e32 v0, v38, v38
	v_min_f32_e32 v33, v37, v0
	v_max_f32_e32 v19, v37, v0
	s_waitcnt lgkmcnt(0)
	v_max3_f32 v35, v33, v21, v35
	v_mov_b32_dpp v21, v17 quad_perm:[1,0,3,2] row_mask:0xf bank_mask:0xf bound_ctrl:1
	v_max_f32_e32 v21, v21, v21
	v_min_f32_e32 v33, v17, v21
	v_max_f32_e32 v21, v17, v21
	v_max_f32_e32 v9, v33, v9
	v_pk_add_f32 v[18:19], v[18:19], v[34:35]
	v_mov_b32_dpp v33, v21 quad_perm:[2,3,0,1] row_mask:0xf bank_mask:0xf bound_ctrl:1
	v_max_f32_e32 v33, v33, v33
	v_min_f32_e32 v35, v21, v33
	v_max_f32_e32 v21, v21, v33
	v_mov_b32_dpp v34, v9 quad_perm:[2,3,0,1] row_mask:0xf bank_mask:0xf bound_ctrl:1
	v_max3_f32 v9, v35, v9, v34
	v_mov_b32_dpp v33, v21 row_half_mirror row_mask:0xf bank_mask:0xf bound_ctrl:1
	v_max_f32_e32 v33, v33, v33
	v_min_f32_e32 v35, v21, v33
	v_max_f32_e32 v21, v21, v33
	v_mov_b32_dpp v34, v9 row_half_mirror row_mask:0xf bank_mask:0xf bound_ctrl:1
	v_max3_f32 v9, v35, v9, v34
	v_mov_b32_dpp v33, v21 row_mirror row_mask:0xf bank_mask:0xf bound_ctrl:1
	v_max_f32_e32 v33, v33, v33
	v_max_f32_e32 v35, v21, v33
	v_mov_b32_dpp v34, v9 row_mirror row_mask:0xf bank_mask:0xf bound_ctrl:1
	ds_bpermute_b32 v36, v3, v35
	v_min_f32_e32 v21, v21, v33
	v_max3_f32 v33, v21, v9, v34
	ds_bpermute_b32 v34, v3, v33
	ds_bpermute_b32 v0, v23, v18
	s_waitcnt lgkmcnt(2)
	v_max_f32_e32 v21, v36, v36
	v_min_f32_e32 v36, v35, v21
	v_max_f32_e32 v21, v35, v21
	s_waitcnt lgkmcnt(1)
	v_max3_f32 v33, v36, v33, v34
	v_pk_add_f32 v[20:21], v[20:21], v[32:33]
	ds_bpermute_b32 v9, v23, v19
	ds_bpermute_b32 v36, v23, v20
	ds_bpermute_b32 v32, v23, v21
	s_and_saveexec_b64 s[28:29], s[2:3]
	s_xor_b64 s[28:29], exec, s[28:29]
	s_cbranch_execz .LBB0_2165
	s_waitcnt lgkmcnt(1)
	v_cmp_le_f32_e32 vcc, v21, v36
	v_cmp_le_f32_e64 s[26:27], v20, v36
	s_nop 0
	v_cndmask_b32_e64 v33, 0, 1, vcc
	v_cmp_ge_f32_e32 vcc, v20, v21
	s_nop 1
	v_cndmask_b32_e64 v34, 0, 1, vcc
	v_cmp_le_f32_e32 vcc, v21, v0
	s_nop 1
	v_addc_co_u32_e32 v33, vcc, v33, v34, vcc
	v_cmp_ge_f32_e32 vcc, v18, v21
	s_nop 1
	v_cndmask_b32_e64 v34, 0, 1, vcc
	v_cmp_le_f32_e32 vcc, v21, v9
	s_nop 1
	v_addc_co_u32_e32 v33, vcc, v33, v34, vcc
	v_cmp_ge_f32_e32 vcc, v19, v21
	s_nop 1
	v_cndmask_b32_e64 v34, 0, 1, vcc
	s_waitcnt lgkmcnt(0)
	v_cmp_le_f32_e32 vcc, v21, v32
	s_nop 1
	v_addc_co_u32_e32 v33, vcc, v33, v34, vcc
	v_cmp_le_f32_e32 vcc, v19, v36
	s_nop 1
	v_cndmask_b32_e64 v34, 0, 1, vcc
	v_cmp_ge_f32_e32 vcc, v20, v19
	s_nop 1
	v_cndmask_b32_e64 v35, 0, 1, vcc
	v_cmp_le_f32_e32 vcc, v19, v0
	s_nop 1
	v_addc_co_u32_e32 v34, vcc, v34, v35, vcc
	v_cmp_ge_f32_e32 vcc, v18, v19
	s_nop 1
	v_cndmask_b32_e64 v35, 0, 1, vcc
	v_cmp_le_f32_e32 vcc, v19, v9
	s_nop 1
	v_addc_co_u32_e32 v34, vcc, v34, v35, vcc
	v_cmp_lt_f32_e32 vcc, v19, v32
	s_nop 1
	v_cndmask_b32_e64 v35, 0, 1, vcc
	v_cmp_gt_f32_e32 vcc, v21, v19
	s_nop 1
	v_addc_co_u32_e32 v34, vcc, v34, v35, vcc
	v_cmp_le_f32_e32 vcc, v18, v36
	s_nop 1
	v_cndmask_b32_e64 v35, 0, 1, vcc
	v_cmp_ge_f32_e32 vcc, v20, v18
	s_nop 1
	v_cndmask_b32_e64 v36, 0, 1, vcc
	v_cmp_le_f32_e32 vcc, v18, v0
	s_nop 1
	v_addc_co_u32_e32 v35, vcc, v35, v36, vcc
	v_cmp_lt_f32_e32 vcc, v18, v9
	s_nop 1
	v_cndmask_b32_e64 v36, 0, 1, vcc
	v_cmp_gt_f32_e32 vcc, v19, v18
	s_nop 1
	v_addc_co_u32_e32 v35, vcc, v35, v36, vcc
	v_cmp_lt_f32_e32 vcc, v18, v32
	s_nop 1
	v_cndmask_b32_e64 v36, 0, 1, vcc
	v_cmp_gt_f32_e32 vcc, v21, v18
	s_nop 1
	v_addc_co_u32_e32 v35, vcc, v35, v36, vcc
